# baseline (speedup 1.0000x reference)
.LBB1_2:
	s_or_b64 exec, exec, s[8:9]
	s_ashr_i32 s9, s2, 3
	s_and_b32 s8, s2, 7
	s_and_b32 s9, s9, -8
	s_bfe_u32 s20, s3, 0x20006
	s_or_b32 s10, s9, s8
	s_lshl_b32 s2, s2, 4
	s_lshr_b32 s22, s3, 6
	v_bfe_u32 v1, v0, 5, 1
	s_and_b32 s2, s2, 0x380
	s_lshl_b32 s8, s20, 5
	s_ashr_i32 s11, s10, 31
	s_or_b32 s2, s8, s2
	s_lshl_b64 s[8:9], s[10:11], 19
	v_lshl_or_b32 v2, s22, 1, v1
	s_waitcnt lgkmcnt(0)
	s_cmpk_gt_u32 s3, 0xff
	s_cselect_b32 s44, s46, s44
	s_cselect_b32 s45, s47, s45
	v_and_b32_e32 v108, 0xff, v0
	v_lshlrev_b32_e32 v108, 2, v108
	global_load_dword v108, v108, s[44:45]
	s_add_u32 s14, s4, s8
	v_lshlrev_b32_e32 v6, 9, v2
	v_lshlrev_b32_e32 v2, 2, v2
	v_and_b32_e32 v5, 31, v0
	s_addc_u32 s15, s5, s9
	v_and_b32_e32 v2, 12, v2
	s_bfe_u32 s4, s3, 0x20007
	v_bitop3_b32 v2, v2, v5, s4 bitop3:0x36
	s_lshl_b32 s4, s22, 10
	v_lshl_or_b32 v192, v2, 4, v6
	s_add_i32 s21, s4, 0
	s_and_b32 s4, s2, 0x380
	s_lshl_b32 s4, s4, 9
	s_add_u32 s4, s14, s4
	s_addc_u32 s5, s15, 0
	s_add_i32 s27, s21, 0x10000
	s_add_i32 s28, s21, 0x12000
	s_add_i32 s29, s21, 0x14000
	s_add_i32 s30, s21, 0x16000
	s_mov_b32 s8, m0
	s_mov_b32 m0, s27
	s_nop 0
	global_load_lds_dwordx4 v192, s[4:5]
	s_mov_b32 m0, s8
	s_add_u32 s40, s4, 0x2000
	s_addc_u32 s41, s5, 0
	s_mov_b32 s8, m0
	s_mov_b32 m0, s28
	s_nop 0
	global_load_lds_dwordx4 v192, s[40:41]
	s_mov_b32 m0, s8
	s_add_u32 s40, s4, 0x4000
	s_addc_u32 s41, s5, 0
	s_mov_b32 s8, m0
	s_mov_b32 m0, s29
	s_nop 0
	global_load_lds_dwordx4 v192, s[40:41]
	s_mov_b32 m0, s8
	s_add_u32 s40, s4, 0x6000
	s_addc_u32 s41, s5, 0
	s_mov_b32 s8, m0
	s_mov_b32 m0, s30
	s_nop 0
	global_load_lds_dwordx4 v192, s[40:41]
	s_mov_b32 m0, s8
	s_add_u32 s40, s4, 0x8000
	s_addc_u32 s41, s5, 0
	s_add_i32 s42, s21, 0x18000
	s_mov_b32 s8, m0
	s_mov_b32 m0, s42
	s_nop 0
	global_load_lds_dwordx4 v192, s[40:41]
	s_mov_b32 m0, s8
	s_add_u32 s40, s4, 0xa000
	s_addc_u32 s41, s5, 0
	s_add_i32 s42, s21, 0x1a000
	s_mov_b32 s8, m0
	s_mov_b32 m0, s42
	s_nop 0
	global_load_lds_dwordx4 v192, s[40:41]
	s_mov_b32 m0, s8
	s_add_u32 s40, s4, 0xc000
	s_addc_u32 s41, s5, 0
	s_add_i32 s42, s21, 0x1c000
	s_mov_b32 s8, m0
	s_mov_b32 m0, s42
	s_nop 0
	global_load_lds_dwordx4 v192, s[40:41]
	s_mov_b32 m0, s8
	s_add_u32 s40, s4, 0xe000
	s_addc_u32 s41, s5, 0
	s_add_i32 s42, s21, 0x1e000
	s_mov_b32 s8, m0
	s_mov_b32 m0, s42
	s_nop 0
	global_load_lds_dwordx4 v192, s[40:41]
	s_mov_b32 m0, s8
	s_mov_b32 s4, m0
	s_mov_b32 m0, s21
	s_nop 0
	global_load_lds_dwordx4 v192, s[6:7]
	s_mov_b32 m0, s4
	s_add_u32 s4, s6, 0x2000
	s_addc_u32 s5, s7, 0
	s_add_i32 s31, s21, 0x2000
	s_mov_b32 s8, m0
	s_mov_b32 m0, s31
	s_nop 0
	global_load_lds_dwordx4 v192, s[4:5]
	s_mov_b32 m0, s8
	s_add_u32 s4, s6, 0x4000
	s_addc_u32 s5, s7, 0
	s_add_i32 s33, s21, 0x4000
	s_mov_b32 s8, m0
	s_mov_b32 m0, s33
	s_nop 0
	global_load_lds_dwordx4 v192, s[4:5]
	s_mov_b32 m0, s8
	s_add_u32 s4, s6, 0x6000
	s_addc_u32 s5, s7, 0
	s_add_i32 s34, s21, 0x6000
	s_mov_b32 s8, m0
	s_mov_b32 m0, s34
	s_nop 0
	global_load_lds_dwordx4 v192, s[4:5]
	s_mov_b32 m0, s8
	s_add_u32 s4, s6, 0x8000
	s_addc_u32 s5, s7, 0
	s_add_i32 s23, s21, 0x8000
	s_mov_b32 s8, m0
	s_mov_b32 m0, s23
	s_nop 0
	global_load_lds_dwordx4 v192, s[4:5]
	s_mov_b32 m0, s8
	s_add_u32 s4, s6, 0xa000
	s_addc_u32 s5, s7, 0
	s_add_i32 s24, s21, 0xa000
	s_mov_b32 s8, m0
	s_mov_b32 m0, s24
	s_nop 0
	global_load_lds_dwordx4 v192, s[4:5]
	s_mov_b32 m0, s8
	s_add_u32 s4, s6, 0xc000
	s_addc_u32 s5, s7, 0
	s_add_i32 s25, s21, 0xc000
	s_mov_b32 s8, m0
	s_mov_b32 m0, s25
	s_nop 0
	global_load_lds_dwordx4 v192, s[4:5]
	s_mov_b32 m0, s8
	s_add_u32 s4, s6, 0xe000
	s_addc_u32 s5, s7, 0
	s_add_i32 s26, s21, 0xe000
	s_mov_b32 s8, m0
	s_mov_b32 m0, s26
	s_nop 0
	global_load_lds_dwordx4 v192, s[4:5]
	s_mov_b32 m0, s8
	s_load_dwordx2 s[8:9], s[0:1], 0x18
	s_load_dwordx2 s[12:13], s[0:1], 0x28
	v_and_b32_e32 v81, 63, v0
	v_lshlrev_b32_e32 v2, 2, v0
	v_add_u32_e32 v6, 0x22000, v2
	s_waitcnt vmcnt(16)
	ds_write_b32 v6, v108
	s_lshr_b32 s5, s3, 8
	s_lshl_b32 s16, s20, 12
	s_lshl_b32 s4, s5, 5
	s_add_i32 s35, s16, 0
	s_add_u32 s18, s6, 0x18000
	v_and_b32_e32 v2, 12, v2
	v_bfe_u32 v0, v0, 2, 2
	s_addc_u32 s19, s7, 0
	v_bitop3_b32 v0, v2, v1, v0 bitop3:0x36
	s_add_u32 s16, s14, 0x8000
	v_lshlrev_b32_e32 v100, 4, v0
	v_or_b32_e32 v0, s4, v5
	s_addc_u32 s17, s15, 0
	s_lshl_b32 s36, s5, 7
	v_lshl_add_u32 v101, v0, 9, 0
	v_lshl_or_b32 v0, v1, 4, s36
	v_add_u32_e32 v0, 0, v0
	v_add_u32_e32 v83, v101, v100
	s_waitcnt vmcnt(4)
	s_waitcnt lgkmcnt(0)
	s_barrier
	s_lshl_b32 s40, s20, 14
	s_add_i32 s40, s40, 0x10000
	v_lshl_add_u32 v108, v5, 9, s40
	v_add_u32_e32 v109, v108, v100
	ds_read_b128 v[68:71], v109
	ds_read_b128 v[76:79], v109 offset:256
	v_xor_b32_e32 v109, 0x20, v100
	v_add_u32_e32 v109, v108, v109
	ds_read_b128 v[60:63], v109
	ds_read_b128 v[72:75], v109 offset:256
	v_xor_b32_e32 v109, 0x40, v100
	v_add_u32_e32 v109, v108, v109
	ds_read_b128 v[52:55], v109
	ds_read_b128 v[64:67], v109 offset:256
	v_xor_b32_e32 v109, 0x60, v100
	v_add_u32_e32 v109, v108, v109
	ds_read_b128 v[48:51], v109
	ds_read_b128 v[56:59], v109 offset:256
	v_xor_b32_e32 v109, 0x80, v100
	v_add_u32_e32 v109, v108, v109
	ds_read_b128 v[36:39], v109
	ds_read_b128 v[44:47], v109 offset:256
	v_xor_b32_e32 v109, 0xa0, v100
	v_add_u32_e32 v109, v108, v109
	ds_read_b128 v[28:31], v109
	ds_read_b128 v[40:43], v109 offset:256
	v_xor_b32_e32 v109, 0xc0, v100
	v_add_u32_e32 v109, v108, v109
	ds_read_b128 v[24:27], v109
	ds_read_b128 v[32:35], v109 offset:256
	v_xor_b32_e32 v109, 0xe0, v100
	v_add_u32_e32 v109, v108, v109
	ds_read_b128 v[20:23], v109
	ds_read_b128 v[16:19], v109 offset:256
	s_waitcnt vmcnt(0) lgkmcnt(0)
	s_barrier
	s_add_u32 s40, s6, 0x10000
	s_addc_u32 s41, s7, 0
	s_mov_b32 s42, m0
	s_mov_b32 m0, s27
	s_nop 0
	global_load_lds_dwordx4 v192, s[40:41]
	s_mov_b32 m0, s42
	s_add_u32 s40, s6, 0x12000
	s_addc_u32 s41, s7, 0
	s_mov_b32 s42, m0
	s_mov_b32 m0, s28
	s_nop 0
	global_load_lds_dwordx4 v192, s[40:41]
	s_mov_b32 m0, s42
	s_add_u32 s40, s6, 0x14000
	s_addc_u32 s41, s7, 0
	s_mov_b32 s42, m0
	s_mov_b32 m0, s29
	s_nop 0
	global_load_lds_dwordx4 v192, s[40:41]
	s_mov_b32 m0, s42
	s_add_u32 s40, s6, 0x16000
	s_addc_u32 s41, s7, 0
	s_mov_b32 s42, m0
	s_mov_b32 m0, s30
	s_nop 0
	global_load_lds_dwordx4 v192, s[40:41]
	s_mov_b32 m0, s42
	v_add_u32_e32 v80, 0x22000, v0
	v_lshl_add_u32 v81, v81, 4, s35
	v_add_u32_e32 v81, 0x18000, v81
	v_lshl_add_u32 v82, s5, 11, v81
	ds_read_b128 v[0:3], v80 offset:0
	ds_read_b128 v[4:7], v80 offset:32
	ds_read_b128 v[8:11], v80 offset:64
	ds_read_b128 v[12:15], v80 offset:96
	ds_read_b128 v[108:111], v80 offset:256
	ds_read_b128 v[112:115], v80 offset:288
	ds_read_b128 v[116:119], v80 offset:320
	ds_read_b128 v[120:123], v80 offset:352
	v_xor_b32_e32 v84, 0x20, v100
	v_add_u32_e32 v84, v101, v84
	v_xor_b32_e32 v85, 0x40, v100
	v_add_u32_e32 v85, v101, v85
	v_xor_b32_e32 v86, 0x60, v100
	v_add_u32_e32 v86, v101, v86
	v_xor_b32_e32 v87, 0x80, v100
	v_add_u32_e32 v87, v101, v87
	v_xor_b32_e32 v88, 0xa0, v100
	v_add_u32_e32 v88, v101, v88
	v_xor_b32_e32 v89, 0xc0, v100
	v_add_u32_e32 v89, v101, v89
	v_xor_b32_e32 v90, 0xe0, v100
	v_add_u32_e32 v90, v101, v90
	v_add_u32_e32 v208, 0x10000, v83
	v_add_u32_e32 v209, 0x10000, v84
	v_add_u32_e32 v210, 0x10000, v85
	v_add_u32_e32 v211, 0x10000, v86
	v_add_u32_e32 v212, 0x10000, v87
	v_add_u32_e32 v213, 0x10000, v88
	v_add_u32_e32 v214, 0x10000, v89
	v_add_u32_e32 v215, 0x10000, v90
	ds_read_b128 v[92:95], v83
	ds_read_b128 v[96:99], v83 offset:256
	ds_read_b128 v[200:203], v84
	ds_read_b128 v[204:207], v84 offset:256
	s_waitcnt lgkmcnt(8)
	s_waitcnt lgkmcnt(3)
	v_mfma_f32_32x32x16_bf16 v[0:15], v[92:95], v[68:71], v[0:15]
	s_waitcnt lgkmcnt(2)
	v_mfma_f32_32x32x16_bf16 v[0:15], v[96:99], v[76:79], v[0:15]
	ds_read_b128 v[92:95], v85
	ds_read_b128 v[96:99], v85 offset:256
	s_waitcnt lgkmcnt(3)
	v_mfma_f32_32x32x16_bf16 v[0:15], v[200:203], v[60:63], v[0:15]
	s_waitcnt lgkmcnt(2)
	v_mfma_f32_32x32x16_bf16 v[0:15], v[204:207], v[72:75], v[0:15]
	ds_read_b128 v[200:203], v86
	ds_read_b128 v[204:207], v86 offset:256
	s_waitcnt lgkmcnt(3)
	v_mfma_f32_32x32x16_bf16 v[0:15], v[92:95], v[52:55], v[0:15]
	s_waitcnt lgkmcnt(2)
	v_mfma_f32_32x32x16_bf16 v[0:15], v[96:99], v[64:67], v[0:15]
	ds_read_b128 v[92:95], v87
	ds_read_b128 v[96:99], v87 offset:256
	s_waitcnt lgkmcnt(3)
	v_mfma_f32_32x32x16_bf16 v[0:15], v[200:203], v[48:51], v[0:15]
	s_waitcnt lgkmcnt(2)
	v_mfma_f32_32x32x16_bf16 v[0:15], v[204:207], v[56:59], v[0:15]
	ds_read_b128 v[200:203], v88
	ds_read_b128 v[204:207], v88 offset:256
	s_waitcnt lgkmcnt(3)
	v_mfma_f32_32x32x16_bf16 v[0:15], v[92:95], v[36:39], v[0:15]
	s_waitcnt lgkmcnt(2)
	v_mfma_f32_32x32x16_bf16 v[0:15], v[96:99], v[44:47], v[0:15]
	ds_read_b128 v[92:95], v89
	ds_read_b128 v[96:99], v89 offset:256
	s_waitcnt lgkmcnt(3)
	v_mfma_f32_32x32x16_bf16 v[0:15], v[200:203], v[28:31], v[0:15]
	s_waitcnt lgkmcnt(2)
	v_mfma_f32_32x32x16_bf16 v[0:15], v[204:207], v[40:43], v[0:15]
	ds_read_b128 v[200:203], v90
	ds_read_b128 v[204:207], v90 offset:256
	s_waitcnt lgkmcnt(3)
	v_mfma_f32_32x32x16_bf16 v[0:15], v[92:95], v[24:27], v[0:15]
	s_waitcnt lgkmcnt(2)
	v_mfma_f32_32x32x16_bf16 v[0:15], v[96:99], v[32:35], v[0:15]
	ds_read_b128 v[92:95], v83 offset:32768
	ds_read_b128 v[96:99], v83 offset:33024
	s_waitcnt lgkmcnt(3)
	v_mfma_f32_32x32x16_bf16 v[0:15], v[200:203], v[20:23], v[0:15]
	s_waitcnt lgkmcnt(2)
	v_mfma_f32_32x32x16_bf16 v[0:15], v[204:207], v[16:19], v[0:15]
	ds_read_b128 v[200:203], v84 offset:32768
	ds_read_b128 v[204:207], v84 offset:33024
	s_waitcnt lgkmcnt(15)
	s_waitcnt lgkmcnt(3)
	v_mfma_f32_32x32x16_bf16 v[108:123], v[92:95], v[68:71], v[108:123]
	s_waitcnt lgkmcnt(2)
	v_mfma_f32_32x32x16_bf16 v[108:123], v[96:99], v[76:79], v[108:123]
	ds_read_b128 v[92:95], v85 offset:32768
	ds_read_b128 v[96:99], v85 offset:33024
	s_waitcnt lgkmcnt(3)
	v_mfma_f32_32x32x16_bf16 v[108:123], v[200:203], v[60:63], v[108:123]
	s_waitcnt lgkmcnt(2)
	v_mfma_f32_32x32x16_bf16 v[108:123], v[204:207], v[72:75], v[108:123]
	ds_read_b128 v[200:203], v86 offset:32768
	ds_read_b128 v[204:207], v86 offset:33024
	s_nop 1
	v_cvt_pk_bf16_f32 v216, v0, v1
	v_cvt_pk_bf16_f32 v217, v2, v3
	v_cvt_pk_bf16_f32 v218, v4, v5
	v_cvt_pk_bf16_f32 v219, v6, v7
	s_waitcnt lgkmcnt(3)
	v_mfma_f32_32x32x16_bf16 v[108:123], v[92:95], v[52:55], v[108:123]
	s_waitcnt lgkmcnt(2)
	v_mfma_f32_32x32x16_bf16 v[108:123], v[96:99], v[64:67], v[108:123]
	ds_read_b128 v[92:95], v87 offset:32768
	ds_read_b128 v[96:99], v87 offset:33024
	v_cvt_pk_bf16_f32 v220, v8, v9
	v_cvt_pk_bf16_f32 v221, v10, v11
	v_cvt_pk_bf16_f32 v222, v12, v13
	v_cvt_pk_bf16_f32 v223, v14, v15
	ds_write_b128 v82, v[216:219]
	ds_write_b128 v82, v[220:223] offset:1024
	s_waitcnt lgkmcnt(5)
	v_mfma_f32_32x32x16_bf16 v[108:123], v[200:203], v[48:51], v[108:123]
	s_waitcnt lgkmcnt(4)
	v_mfma_f32_32x32x16_bf16 v[108:123], v[204:207], v[56:59], v[108:123]
	ds_read_b128 v[200:203], v88 offset:32768
	ds_read_b128 v[204:207], v88 offset:33024
	s_waitcnt vmcnt(0)
	s_waitcnt lgkmcnt(2)
	s_barrier
	s_add_u32 s40, s6, 0x18000
	s_addc_u32 s41, s7, 0
	s_mov_b32 s42, m0
	s_mov_b32 m0, s21
	s_nop 0
	global_load_lds_dwordx4 v192, s[40:41]
	s_mov_b32 m0, s42
	s_add_u32 s40, s6, 0x1a000
	s_addc_u32 s41, s7, 0
	s_mov_b32 s42, m0
	s_mov_b32 m0, s31
	s_nop 0
	global_load_lds_dwordx4 v192, s[40:41]
	s_mov_b32 m0, s42
	s_waitcnt lgkmcnt(5)
	v_mfma_f32_32x32x16_bf16 v[108:123], v[92:95], v[36:39], v[108:123]
	s_waitcnt lgkmcnt(4)
	v_mfma_f32_32x32x16_bf16 v[108:123], v[96:99], v[44:47], v[108:123]
	ds_read_b128 v[92:95], v89 offset:32768
	ds_read_b128 v[96:99], v89 offset:33024
	s_add_u32 s40, s6, 0x1c000
	s_addc_u32 s41, s7, 0
	s_mov_b32 s42, m0
	s_mov_b32 m0, s33
	s_nop 0
	global_load_lds_dwordx4 v192, s[40:41]
	s_mov_b32 m0, s42
	s_add_u32 s40, s6, 0x1e000
	s_addc_u32 s41, s7, 0
	s_mov_b32 s42, m0
	s_mov_b32 m0, s34
	s_nop 0
	global_load_lds_dwordx4 v192, s[40:41]
	s_mov_b32 m0, s42
	ds_read_b128 v[128:131], v81
	ds_read_b128 v[132:135], v81 offset:1024
	ds_read_b128 v[136:139], v81 offset:2048
	ds_read_b128 v[140:143], v81 offset:3072
	s_waitcnt lgkmcnt(7)
	v_mfma_f32_32x32x16_bf16 v[108:123], v[200:203], v[28:31], v[108:123]
	s_waitcnt lgkmcnt(6)
	v_mfma_f32_32x32x16_bf16 v[108:123], v[204:207], v[40:43], v[108:123]
	ds_read_b128 v[200:203], v90 offset:32768
	ds_read_b128 v[204:207], v90 offset:33024
	ds_read_b128 v[0:3], v80 offset:512
	ds_read_b128 v[4:7], v80 offset:544
	ds_read_b128 v[8:11], v80 offset:576
	ds_read_b128 v[12:15], v80 offset:608
	s_waitcnt lgkmcnt(11)
	v_mfma_f32_32x32x16_bf16 v[108:123], v[92:95], v[24:27], v[108:123]
	s_waitcnt lgkmcnt(10)
	v_mfma_f32_32x32x16_bf16 v[108:123], v[96:99], v[32:35], v[108:123]
	ds_read_b128 v[92:95], v208
	ds_read_b128 v[96:99], v208 offset:256
	s_waitcnt lgkmcnt(7)
	v_mfma_f32_32x32x16_bf16 v[108:123], v[200:203], v[20:23], v[108:123]
	s_waitcnt lgkmcnt(6)
	v_mfma_f32_32x32x16_bf16 v[108:123], v[204:207], v[16:19], v[108:123]
	ds_read_b128 v[200:203], v209
	ds_read_b128 v[204:207], v209 offset:256
	s_waitcnt lgkmcnt(4)
	s_waitcnt lgkmcnt(3)
	v_mfma_f32_32x32x16_bf16 v[0:15], v[92:95], v[68:71], v[0:15]
	s_waitcnt lgkmcnt(2)
	v_mfma_f32_32x32x16_bf16 v[0:15], v[96:99], v[76:79], v[0:15]
	ds_read_b128 v[92:95], v210
	ds_read_b128 v[96:99], v210 offset:256
	s_waitcnt lgkmcnt(3)
	v_mfma_f32_32x32x16_bf16 v[0:15], v[200:203], v[60:63], v[0:15]
	s_waitcnt lgkmcnt(2)
	v_mfma_f32_32x32x16_bf16 v[0:15], v[204:207], v[72:75], v[0:15]
	ds_read_b128 v[200:203], v211
	ds_read_b128 v[204:207], v211 offset:256
	s_nop 1
	v_cvt_pk_bf16_f32 v216, v108, v109
	v_cvt_pk_bf16_f32 v217, v110, v111
	v_cvt_pk_bf16_f32 v218, v112, v113
	v_cvt_pk_bf16_f32 v219, v114, v115
	s_waitcnt lgkmcnt(3)
	v_mfma_f32_32x32x16_bf16 v[0:15], v[92:95], v[52:55], v[0:15]
	s_waitcnt lgkmcnt(2)
	v_mfma_f32_32x32x16_bf16 v[0:15], v[96:99], v[64:67], v[0:15]
	ds_read_b128 v[92:95], v212
	ds_read_b128 v[96:99], v212 offset:256
	v_cvt_pk_bf16_f32 v220, v116, v117
	v_cvt_pk_bf16_f32 v221, v118, v119
	v_cvt_pk_bf16_f32 v222, v120, v121
	v_cvt_pk_bf16_f32 v223, v122, v123
	ds_write_b128 v82, v[216:219] offset:20480
	ds_write_b128 v82, v[220:223] offset:21504
	s_waitcnt lgkmcnt(5)
	v_mfma_f32_32x32x16_bf16 v[0:15], v[200:203], v[48:51], v[0:15]
	s_waitcnt lgkmcnt(4)
	v_mfma_f32_32x32x16_bf16 v[0:15], v[204:207], v[56:59], v[0:15]
	ds_read_b128 v[200:203], v213
	ds_read_b128 v[204:207], v213 offset:256
	s_waitcnt vmcnt(0)
	s_waitcnt lgkmcnt(2)
	s_barrier
	s_add_u32 s40, s14, 0x0
	s_addc_u32 s41, s15, 0
	s_mov_b32 s42, m0
	s_mov_b32 m0, s23
	s_nop 0
	global_load_lds_dwordx4 v192, s[40:41]
	s_mov_b32 m0, s42
	s_add_u32 s40, s14, 0x2000
	s_addc_u32 s41, s15, 0
	s_mov_b32 s42, m0
	s_mov_b32 m0, s24
	s_nop 0
	global_load_lds_dwordx4 v192, s[40:41]
	s_mov_b32 m0, s42
	s_waitcnt lgkmcnt(5)
	v_mfma_f32_32x32x16_bf16 v[0:15], v[92:95], v[36:39], v[0:15]
	s_waitcnt lgkmcnt(4)
	v_mfma_f32_32x32x16_bf16 v[0:15], v[96:99], v[44:47], v[0:15]
	ds_read_b128 v[92:95], v214
	ds_read_b128 v[96:99], v214 offset:256
	s_add_u32 s40, s14, 0x4000
	s_addc_u32 s41, s15, 0
	s_mov_b32 s42, m0
	s_mov_b32 m0, s25
	s_nop 0
	global_load_lds_dwordx4 v192, s[40:41]
	s_mov_b32 m0, s42
	s_add_u32 s40, s14, 0x6000
	s_addc_u32 s41, s15, 0
	s_mov_b32 s42, m0
	s_mov_b32 m0, s26
	s_nop 0
	global_load_lds_dwordx4 v192, s[40:41]
	s_mov_b32 m0, s42
	ds_read_b128 v[144:147], v81 offset:20480
	ds_read_b128 v[148:151], v81 offset:21504
	ds_read_b128 v[152:155], v81 offset:22528
	ds_read_b128 v[156:159], v81 offset:23552
	s_waitcnt lgkmcnt(7)
	v_mfma_f32_32x32x16_bf16 v[0:15], v[200:203], v[28:31], v[0:15]
	s_waitcnt lgkmcnt(6)
	v_mfma_f32_32x32x16_bf16 v[0:15], v[204:207], v[40:43], v[0:15]
	ds_read_b128 v[200:203], v215
	ds_read_b128 v[204:207], v215 offset:256
	ds_read_b128 v[108:111], v80 offset:768
	ds_read_b128 v[112:115], v80 offset:800
	ds_read_b128 v[116:119], v80 offset:832
	ds_read_b128 v[120:123], v80 offset:864
	s_waitcnt lgkmcnt(11)
	v_mfma_f32_32x32x16_bf16 v[0:15], v[92:95], v[24:27], v[0:15]
	s_waitcnt lgkmcnt(10)
	v_mfma_f32_32x32x16_bf16 v[0:15], v[96:99], v[32:35], v[0:15]
	ds_read_b128 v[92:95], v83
	ds_read_b128 v[96:99], v83 offset:256
	s_waitcnt lgkmcnt(7)
	v_mfma_f32_32x32x16_bf16 v[0:15], v[200:203], v[20:23], v[0:15]
	s_waitcnt lgkmcnt(6)
	v_mfma_f32_32x32x16_bf16 v[0:15], v[204:207], v[16:19], v[0:15]
	ds_read_b128 v[200:203], v84
	ds_read_b128 v[204:207], v84 offset:256
	s_waitcnt lgkmcnt(4)
	s_waitcnt lgkmcnt(3)
	v_mfma_f32_32x32x16_bf16 v[108:123], v[92:95], v[68:71], v[108:123]
	s_waitcnt lgkmcnt(2)
	v_mfma_f32_32x32x16_bf16 v[108:123], v[96:99], v[76:79], v[108:123]
	ds_read_b128 v[92:95], v85
	ds_read_b128 v[96:99], v85 offset:256
	s_waitcnt lgkmcnt(3)
	v_mfma_f32_32x32x16_bf16 v[108:123], v[200:203], v[60:63], v[108:123]
	s_waitcnt lgkmcnt(2)
	v_mfma_f32_32x32x16_bf16 v[108:123], v[204:207], v[72:75], v[108:123]
	ds_read_b128 v[200:203], v86
	ds_read_b128 v[204:207], v86 offset:256
	s_nop 1
	v_cvt_pk_bf16_f32 v216, v0, v1
	v_cvt_pk_bf16_f32 v217, v2, v3
	v_cvt_pk_bf16_f32 v218, v4, v5
	v_cvt_pk_bf16_f32 v219, v6, v7
	s_waitcnt lgkmcnt(3)
	v_mfma_f32_32x32x16_bf16 v[108:123], v[92:95], v[52:55], v[108:123]
	s_waitcnt lgkmcnt(2)
	v_mfma_f32_32x32x16_bf16 v[108:123], v[96:99], v[64:67], v[108:123]
	ds_read_b128 v[92:95], v87
	ds_read_b128 v[96:99], v87 offset:256
	v_cvt_pk_bf16_f32 v220, v8, v9
	v_cvt_pk_bf16_f32 v221, v10, v11
	v_cvt_pk_bf16_f32 v222, v12, v13
	v_cvt_pk_bf16_f32 v223, v14, v15
	ds_write_b128 v82, v[216:219]
	ds_write_b128 v82, v[220:223] offset:1024
	s_waitcnt lgkmcnt(5)
	v_mfma_f32_32x32x16_bf16 v[108:123], v[200:203], v[48:51], v[108:123]
	s_waitcnt lgkmcnt(4)
	v_mfma_f32_32x32x16_bf16 v[108:123], v[204:207], v[56:59], v[108:123]
	ds_read_b128 v[200:203], v88
	ds_read_b128 v[204:207], v88 offset:256
	s_waitcnt lgkmcnt(2)
	s_barrier
	s_add_u32 s40, s14, 0x8000
	s_addc_u32 s41, s15, 0
	s_mov_b32 s42, m0
	s_mov_b32 m0, s27
	s_nop 0
	global_load_lds_dwordx4 v192, s[40:41]
	s_mov_b32 m0, s42
	s_add_u32 s40, s14, 0xa000
	s_addc_u32 s41, s15, 0
	s_mov_b32 s42, m0
	s_mov_b32 m0, s28
	s_nop 0
	global_load_lds_dwordx4 v192, s[40:41]
	s_mov_b32 m0, s42
	s_waitcnt lgkmcnt(5)
	v_mfma_f32_32x32x16_bf16 v[108:123], v[92:95], v[36:39], v[108:123]
	s_waitcnt lgkmcnt(4)
	v_mfma_f32_32x32x16_bf16 v[108:123], v[96:99], v[44:47], v[108:123]
	ds_read_b128 v[92:95], v89
	ds_read_b128 v[96:99], v89 offset:256
	s_add_u32 s40, s14, 0xc000
	s_addc_u32 s41, s15, 0
	s_mov_b32 s42, m0
	s_mov_b32 m0, s29
	s_nop 0
	global_load_lds_dwordx4 v192, s[40:41]
	s_mov_b32 m0, s42
	s_add_u32 s40, s14, 0xe000
	s_addc_u32 s41, s15, 0
	s_mov_b32 s42, m0
	s_mov_b32 m0, s30
	s_nop 0
	global_load_lds_dwordx4 v192, s[40:41]
	s_mov_b32 m0, s42
	ds_read_b128 v[160:163], v81
	ds_read_b128 v[164:167], v81 offset:1024
	ds_read_b128 v[168:171], v81 offset:2048
	ds_read_b128 v[172:175], v81 offset:3072
	s_waitcnt lgkmcnt(7)
	v_mfma_f32_32x32x16_bf16 v[108:123], v[200:203], v[28:31], v[108:123]
	s_waitcnt lgkmcnt(6)
	v_mfma_f32_32x32x16_bf16 v[108:123], v[204:207], v[40:43], v[108:123]
	ds_read_b128 v[200:203], v90
	ds_read_b128 v[204:207], v90 offset:256
	s_waitcnt lgkmcnt(7)
	v_mfma_f32_32x32x16_bf16 v[108:123], v[92:95], v[24:27], v[108:123]
	s_waitcnt lgkmcnt(6)
	v_mfma_f32_32x32x16_bf16 v[108:123], v[96:99], v[32:35], v[108:123]
	s_waitcnt lgkmcnt(1)
	v_mfma_f32_32x32x16_bf16 v[108:123], v[200:203], v[20:23], v[108:123]
	s_waitcnt lgkmcnt(0)
	v_mfma_f32_32x32x16_bf16 v[108:123], v[204:207], v[16:19], v[108:123]
	s_nop 11
	s_nop 2
	v_cvt_pk_bf16_f32 v216, v108, v109
	v_cvt_pk_bf16_f32 v217, v110, v111
	v_cvt_pk_bf16_f32 v218, v112, v113
	v_cvt_pk_bf16_f32 v219, v114, v115
	v_cvt_pk_bf16_f32 v220, v116, v117
	v_cvt_pk_bf16_f32 v221, v118, v119
	v_cvt_pk_bf16_f32 v222, v120, v121
	v_cvt_pk_bf16_f32 v223, v122, v123
	ds_write_b128 v82, v[216:219] offset:20480
	ds_write_b128 v82, v[220:223] offset:21504
	v_mbcnt_lo_u32_b32 v224, -1, 0
	v_mbcnt_hi_u32_b32 v193, -1, v224
	v_mov_b32_e32 v194, v193
	s_waitcnt vmcnt(4) lgkmcnt(0)
	s_barrier
	ds_read_b128 v[176:179], v81 offset:20480
	ds_read_b128 v[180:183], v81 offset:21504
	ds_read_b128 v[184:187], v81 offset:22528
	ds_read_b128 v[188:191], v81 offset:23552
	s_movk_i32 s7, 0x80
	s_movk_i32 s6, 0xc0
	s_mov_b32 s5, 0x10000
	s_waitcnt lgkmcnt(0)
	s_barrier
	s_cmpk_gt_u32 s3, 0xff
	s_nop 0
	v_and_b32_e32 v196, 31, v194
	v_ashrrev_i32_e32 v197, 5, v194
	v_lshlrev_b32_e32 v195, 2, v194
	v_bfe_u32 v198, v194, 2, 2
	s_cbranch_scc0 .LBB1_16
	v_lshl_add_u32 v0, s20, 2, v197
	v_lshlrev_b32_e32 v3, 2, v197
	v_add_u32_e32 v1, 2, v0
	v_lshlrev_b32_e32 v2, 9, v0
	v_and_b32_e32 v3, 12, v3
	v_bfe_u32 v0, v0, 2, 2
	v_bitop3_b32 v0, v0, v196, v3 bitop3:0x36
	v_lshl_or_b32 v199, v0, 4, v2
	v_lshlrev_b32_e32 v0, 2, v1
	s_bfe_u32 s18, s3, 0x10006
	v_and_b32_e32 v0, 12, v0
	v_bfe_u32 v2, v1, 2, 2
	v_bitop3_b32 v0, v0, v196, v2 bitop3:0x36
	v_lshrrev_b32_e32 v2, 3, v194
	s_lshl_b32 s16, s18, 8
	v_and_b32_e32 v2, 2, v2
	v_bfe_u32 v3, v194, 1, 1
	s_add_i32 s16, s16, 0
	v_lshlrev_b32_e32 v4, 3, v194
	v_lshl_add_u32 v5, v197, 11, s16
	v_bitop3_b32 v2, v2, v197, v3 bitop3:0x36
	v_and_or_b32 v4, v4, 8, v5
	v_lshlrev_b32_e32 v2, 4, v2
	v_lshlrev_b32_e32 v3, 6, v198
	v_lshl_add_u32 v4, v198, 9, v4
	v_or_b32_e32 v5, v2, v3
	v_add_u32_e32 v200, v4, v5
	v_bitop3_b32 v5, v2, v3, 32 bitop3:0xde
	v_add_u32_e32 v6, 0x1000, v4
	v_add_u32_e32 v201, v6, v5
	v_xor_b32_e32 v5, 64, v3
	v_bitop3_b32 v5, v2, v5, 32 bitop3:0xde
	v_add_u32_e32 v203, v6, v5
	v_xor_b32_e32 v5, 0x80, v3
	v_bitop3_b32 v7, v2, v3, 64 bitop3:0xf6
	v_bitop3_b32 v5, v2, v5, 32 bitop3:0xde
	v_add_u32_e32 v202, v4, v7
	v_bitop3_b32 v7, v2, v3, s7 bitop3:0xf6
	v_add_u32_e32 v205, v6, v5
	v_xor_b32_e32 v5, 0xc0, v3
	v_bitop3_b32 v3, v2, v3, s6 bitop3:0xf6
	s_and_b32 s6, s22, 2
	v_lshlrev_b32_e32 v1, 9, v1
	s_lshl_b32 s27, s6, 2
	s_lshl_b32 s7, s6, 8
	s_lshl_b32 s6, s6, 12
	v_lshl_or_b32 v208, v0, 4, v1
	s_lshl_b32 s19, s20, 11
	s_add_i32 s7, s7, 0
	s_add_i32 s6, s6, 0
	v_mov_b32_e32 v0, 0
	v_bitop3_b32 v2, v2, v5, 32 bitop3:0xde
	s_waitcnt vmcnt(0)
	s_add_i32 s19, s19, 0
	s_add_i32 s16, s7, 0x20000
	s_add_i32 s7, s7, 0x20100
	v_lshlrev_b32_e32 v209, 4, v194
	s_add_i32 s6, s6, 0x18000
	v_mov_b32_e32 v14, v0
	v_mov_b32_e32 v15, v0
	v_add_u32_e32 v204, v4, v7
	v_add_u32_e32 v206, v4, v3
	v_add_u32_e32 v207, v6, v2
	v_add_u32_e32 v212, s6, v209
	s_add_u32 s6, s8, 0xfff90000
	v_mov_b32_e32 v1, v0
	v_mov_b32_e32 v2, v0
	v_mov_b32_e32 v3, v0
	v_mov_b32_e32 v4, v0
	v_mov_b32_e32 v5, v0
	v_mov_b32_e32 v6, v0
	v_mov_b32_e32 v7, v0
	v_mov_b32_e32 v8, v0
	v_mov_b32_e32 v9, v0
	v_mov_b32_e32 v10, v0
	v_mov_b32_e32 v11, v0
	v_mov_b32_e32 v12, v0
	v_mov_b32_e32 v13, v0
	v_mov_b64_e32 v[62:63], v[14:15]
	v_mov_b64_e32 v[94:95], v[14:15]
	v_mov_b64_e32 v[126:127], v[14:15]
	v_mov_b64_e32 v[30:31], v[14:15]
	v_mov_b64_e32 v[46:47], v[14:15]
	v_mov_b64_e32 v[78:79], v[14:15]
	v_mov_b64_e32 v[110:111], v[14:15]
	v_add_u32_e32 v210, s16, v195
	v_add_u32_e32 v211, s7, v195
	s_addc_u32 s7, s9, -1
	s_mov_b32 s33, 1
	s_mov_b32 s31, 0x8000
	s_mov_b32 s29, 0x10000
	v_mov_b64_e32 v[60:61], v[12:13]
	v_mov_b64_e32 v[58:59], v[10:11]
	v_mov_b64_e32 v[56:57], v[8:9]
	v_mov_b64_e32 v[54:55], v[6:7]
	v_mov_b64_e32 v[52:53], v[4:5]
	v_mov_b64_e32 v[50:51], v[2:3]
	v_mov_b64_e32 v[48:49], v[0:1]
	v_mov_b64_e32 v[92:93], v[12:13]
	v_mov_b64_e32 v[90:91], v[10:11]
	v_mov_b64_e32 v[88:89], v[8:9]
	v_mov_b64_e32 v[86:87], v[6:7]
	v_mov_b64_e32 v[84:85], v[4:5]
	v_mov_b64_e32 v[82:83], v[2:3]
	v_mov_b64_e32 v[80:81], v[0:1]
	v_mov_b64_e32 v[124:125], v[12:13]
	v_mov_b64_e32 v[122:123], v[10:11]
	v_mov_b64_e32 v[120:121], v[8:9]
	v_mov_b64_e32 v[118:119], v[6:7]
	v_mov_b64_e32 v[116:117], v[4:5]
	v_mov_b64_e32 v[114:115], v[2:3]
	v_mov_b64_e32 v[112:113], v[0:1]
	v_mov_b64_e32 v[28:29], v[12:13]
	v_mov_b64_e32 v[26:27], v[10:11]
	v_mov_b64_e32 v[24:25], v[8:9]
	v_mov_b64_e32 v[22:23], v[6:7]
	v_mov_b64_e32 v[20:21], v[4:5]
	v_mov_b64_e32 v[18:19], v[2:3]
	v_mov_b64_e32 v[16:17], v[0:1]
	v_mov_b64_e32 v[44:45], v[12:13]
	v_mov_b64_e32 v[42:43], v[10:11]
	v_mov_b64_e32 v[40:41], v[8:9]
	v_mov_b64_e32 v[38:39], v[6:7]
	v_mov_b64_e32 v[36:37], v[4:5]
	v_mov_b64_e32 v[34:35], v[2:3]
	v_mov_b64_e32 v[32:33], v[0:1]
	v_mov_b64_e32 v[76:77], v[12:13]
	v_mov_b64_e32 v[74:75], v[10:11]
	v_mov_b64_e32 v[72:73], v[8:9]
	v_mov_b64_e32 v[70:71], v[6:7]
	v_mov_b64_e32 v[68:69], v[4:5]
	v_mov_b64_e32 v[66:67], v[2:3]
	v_mov_b64_e32 v[64:65], v[0:1]
	v_mov_b64_e32 v[108:109], v[12:13]
	v_mov_b64_e32 v[106:107], v[10:11]
	v_mov_b64_e32 v[104:105], v[8:9]
	v_mov_b64_e32 v[102:103], v[6:7]
	v_mov_b64_e32 v[100:101], v[4:5]
	v_mov_b64_e32 v[98:99], v[2:3]
	v_mov_b64_e32 v[96:97], v[0:1]
	s_waitcnt lgkmcnt(0)
	s_barrier
